# baseline (speedup 1.0000x reference)
.Lsc_dskip15:
	s_waitcnt lgkmcnt(0)
	s_barrier
	v_lshlrev_b32_e32 v50, 3, v0
	v_mov_b32_e32 v52, 0
	v_mov_b32_e32 v53, 0
	v_cmp_gt_u32_e32 vcc, 0x224, v0
	s_and_saveexec_b64 s[36:37], vcc
	ds_read_b64 v[52:53], v50 offset:4608
	s_mov_b64 exec, s[36:37]
	s_waitcnt lgkmcnt(0)
	v_add_u32_e32 v54, v52, v53
	v_mov_b32_e32 v55, v54
	s_nop 1
	v_add_u32_dpp v55, v55, v55 row_shr:1 row_mask:0xf bank_mask:0xf bound_ctrl:0
	s_nop 1
	v_add_u32_dpp v55, v55, v55 row_shr:2 row_mask:0xf bank_mask:0xf bound_ctrl:0
	s_nop 1
	v_add_u32_dpp v55, v55, v55 row_shr:4 row_mask:0xf bank_mask:0xf bound_ctrl:0
	s_nop 1
	v_add_u32_dpp v55, v55, v55 row_shr:8 row_mask:0xf bank_mask:0xf bound_ctrl:0
	s_nop 1
	v_add_u32_dpp v55, v55, v55 row_bcast:15 row_mask:0xa bank_mask:0xf
	s_nop 1
	v_add_u32_dpp v55, v55, v55 row_bcast:31 row_mask:0xc bank_mask:0xf
	v_lshrrev_b32_e32 v56, 6, v0
	s_nop 0
	v_readfirstlane_b32 s3, v56
	v_readlane_b32 s14, v55, 63
	s_lshl_b32 s15, s3, 2
	s_add_u32 s15, s15, 0x2400
	v_mov_b32_e32 v57, s14
	v_mov_b32_e32 v58, s15
	s_mov_b64 s[38:39], exec
	s_mov_b64 exec, 1
	ds_write_b32 v58, v57
	s_mov_b64 exec, s[38:39]
	s_waitcnt lgkmcnt(0)
	s_barrier
	v_and_b32_e32 v57, 15, v0
	v_lshlrev_b32_e32 v57, 2, v57
	ds_read_b32 v57, v57 offset:9216
	s_waitcnt lgkmcnt(0)
	s_nop 1
	v_add_u32_dpp v57, v57, v57 row_shr:1 row_mask:0xf bank_mask:0xf bound_ctrl:0
	s_nop 1
	v_add_u32_dpp v57, v57, v57 row_shr:2 row_mask:0xf bank_mask:0xf bound_ctrl:0
	s_nop 1
	v_add_u32_dpp v57, v57, v57 row_shr:4 row_mask:0xf bank_mask:0xf bound_ctrl:0
	s_nop 1
	v_add_u32_dpp v57, v57, v57 row_shr:8 row_mask:0xf bank_mask:0xf bound_ctrl:0
	s_sub_u32 s15, s3, 1
	s_max_i32 s15, s15, 0
	s_nop 1
	v_readlane_b32 s16, v57, s15
	s_cmp_eq_u32 s3, 0
	s_cselect_b32 s16, 0, s16
	v_sub_u32_e32 v58, v55, v54
	v_add_u32_e32 v58, s16, v58
	v_add_u32_e32 v59, v58, v52
	v_cmp_gt_u32_e32 vcc, 0x224, v0
	s_and_saveexec_b64 s[36:37], vcc
	ds_read_b64 v[56:57], v50
	ds_write_b64 v50, v[58:59] offset:9728
	s_waitcnt lgkmcnt(0)
	v_sub_u32_e32 v56, v56, v58
	v_sub_u32_e32 v57, v57, v59
	ds_write_b64 v50, v[56:57]
	s_mov_b64 exec, s[36:37]
	s_waitcnt lgkmcnt(0)
	s_barrier
	v_mov_b32_e32 v60, 0x447
	v_cmp_gt_i32_e64 s[20:21], 0, v3
	v_subrev_co_u32_e32 v51, vcc, 0x61a80, v3
	v_lshrrev_b32_e32 v51, 6, v51
	v_lshrrev_b32_e32 v52, 9, v3
	v_add_u32_e32 v51, 0x30e, v51
	v_cndmask_b32_e32 v51, v51, v52, vcc
	v_cndmask_b32_e64 v51, v51, v60, s[20:21]
	v_lshlrev_b32_e32 v51, 2, v51
	ds_read_b32 v53, v51 offset:9728
	v_cmp_gt_i32_e64 s[20:21], 0, v5
	v_subrev_co_u32_e32 v51, vcc, 0x61a80, v5
	v_lshrrev_b32_e32 v51, 6, v51
	v_lshrrev_b32_e32 v52, 9, v5
	v_add_u32_e32 v51, 0x30e, v51
	v_cndmask_b32_e32 v51, v51, v52, vcc
	v_cndmask_b32_e64 v51, v51, v60, s[20:21]
	v_lshlrev_b32_e32 v51, 2, v51
	ds_read_b32 v54, v51 offset:9728
	v_cmp_gt_i32_e64 s[20:21], 0, v7
	v_subrev_co_u32_e32 v51, vcc, 0x61a80, v7
	v_lshrrev_b32_e32 v51, 6, v51
	v_lshrrev_b32_e32 v52, 9, v7
	v_add_u32_e32 v51, 0x30e, v51
	v_cndmask_b32_e32 v51, v51, v52, vcc
	v_cndmask_b32_e64 v51, v51, v60, s[20:21]
	v_lshlrev_b32_e32 v51, 2, v51
	ds_read_b32 v55, v51 offset:9728
	v_cmp_gt_i32_e64 s[20:21], 0, v9
	v_subrev_co_u32_e32 v51, vcc, 0x61a80, v9
	v_lshrrev_b32_e32 v51, 6, v51
	v_lshrrev_b32_e32 v52, 9, v9
	v_add_u32_e32 v51, 0x30e, v51
	v_cndmask_b32_e32 v51, v51, v52, vcc
	v_cndmask_b32_e64 v51, v51, v60, s[20:21]
	v_lshlrev_b32_e32 v51, 2, v51
	ds_read_b32 v56, v51 offset:9728
	s_waitcnt lgkmcnt(0)
	v_add_u32_e32 v34, v34, v53
	v_add_u32_e32 v35, v35, v54
	v_add_u32_e32 v36, v36, v55
	v_add_u32_e32 v37, v37, v56
	v_cmp_gt_i32_e64 s[20:21], 0, v11
	v_subrev_co_u32_e32 v51, vcc, 0x61a80, v11
	v_lshrrev_b32_e32 v51, 6, v51
	v_lshrrev_b32_e32 v52, 9, v11
	v_add_u32_e32 v51, 0x30e, v51
	v_cndmask_b32_e32 v51, v51, v52, vcc
	v_cndmask_b32_e64 v51, v51, v60, s[20:21]
	v_lshlrev_b32_e32 v51, 2, v51
	ds_read_b32 v53, v51 offset:9728
	v_cmp_gt_i32_e64 s[20:21], 0, v13
	v_subrev_co_u32_e32 v51, vcc, 0x61a80, v13
	v_lshrrev_b32_e32 v51, 6, v51
	v_lshrrev_b32_e32 v52, 9, v13
	v_add_u32_e32 v51, 0x30e, v51
	v_cndmask_b32_e32 v51, v51, v52, vcc
	v_cndmask_b32_e64 v51, v51, v60, s[20:21]
	v_lshlrev_b32_e32 v51, 2, v51
	ds_read_b32 v54, v51 offset:9728
	v_cmp_gt_i32_e64 s[20:21], 0, v15
	v_subrev_co_u32_e32 v51, vcc, 0x61a80, v15
	v_lshrrev_b32_e32 v51, 6, v51
	v_lshrrev_b32_e32 v52, 9, v15
	v_add_u32_e32 v51, 0x30e, v51
	v_cndmask_b32_e32 v51, v51, v52, vcc
	v_cndmask_b32_e64 v51, v51, v60, s[20:21]
	v_lshlrev_b32_e32 v51, 2, v51
	ds_read_b32 v55, v51 offset:9728
	v_cmp_gt_i32_e64 s[20:21], 0, v17
	v_subrev_co_u32_e32 v51, vcc, 0x61a80, v17
	v_lshrrev_b32_e32 v51, 6, v51
	v_lshrrev_b32_e32 v52, 9, v17
	v_add_u32_e32 v51, 0x30e, v51
	v_cndmask_b32_e32 v51, v51, v52, vcc
	v_cndmask_b32_e64 v51, v51, v60, s[20:21]
	v_lshlrev_b32_e32 v51, 2, v51
	ds_read_b32 v56, v51 offset:9728
	s_waitcnt lgkmcnt(0)
	v_add_u32_e32 v38, v38, v53
	v_add_u32_e32 v39, v39, v54
	v_add_u32_e32 v40, v40, v55
	v_add_u32_e32 v41, v41, v56
	v_cmp_gt_i32_e64 s[20:21], 0, v19
	v_subrev_co_u32_e32 v51, vcc, 0x61a80, v19
	v_lshrrev_b32_e32 v51, 6, v51
	v_lshrrev_b32_e32 v52, 9, v19
	v_add_u32_e32 v51, 0x30e, v51
	v_cndmask_b32_e32 v51, v51, v52, vcc
	v_cndmask_b32_e64 v51, v51, v60, s[20:21]
	v_lshlrev_b32_e32 v51, 2, v51
	ds_read_b32 v53, v51 offset:9728
	v_cmp_gt_i32_e64 s[20:21], 0, v21
	v_subrev_co_u32_e32 v51, vcc, 0x61a80, v21
	v_lshrrev_b32_e32 v51, 6, v51
	v_lshrrev_b32_e32 v52, 9, v21
	v_add_u32_e32 v51, 0x30e, v51
	v_cndmask_b32_e32 v51, v51, v52, vcc
	v_cndmask_b32_e64 v51, v51, v60, s[20:21]
	v_lshlrev_b32_e32 v51, 2, v51
	ds_read_b32 v54, v51 offset:9728
	v_cmp_gt_i32_e64 s[20:21], 0, v23
	v_subrev_co_u32_e32 v51, vcc, 0x61a80, v23
	v_lshrrev_b32_e32 v51, 6, v51
	v_lshrrev_b32_e32 v52, 9, v23
	v_add_u32_e32 v51, 0x30e, v51
	v_cndmask_b32_e32 v51, v51, v52, vcc
	v_cndmask_b32_e64 v51, v51, v60, s[20:21]
	v_lshlrev_b32_e32 v51, 2, v51
	ds_read_b32 v55, v51 offset:9728
	v_cmp_gt_i32_e64 s[20:21], 0, v25
	v_subrev_co_u32_e32 v51, vcc, 0x61a80, v25
	v_lshrrev_b32_e32 v51, 6, v51
	v_lshrrev_b32_e32 v52, 9, v25
	v_add_u32_e32 v51, 0x30e, v51
	v_cndmask_b32_e32 v51, v51, v52, vcc
	v_cndmask_b32_e64 v51, v51, v60, s[20:21]
	v_lshlrev_b32_e32 v51, 2, v51
	ds_read_b32 v56, v51 offset:9728
	s_waitcnt lgkmcnt(0)
	v_add_u32_e32 v42, v42, v53
	v_add_u32_e32 v43, v43, v54
	v_add_u32_e32 v44, v44, v55
	v_add_u32_e32 v45, v45, v56
	v_cmp_gt_i32_e64 s[20:21], 0, v27
	v_subrev_co_u32_e32 v51, vcc, 0x61a80, v27
	v_lshrrev_b32_e32 v51, 6, v51
	v_lshrrev_b32_e32 v52, 9, v27
	v_add_u32_e32 v51, 0x30e, v51
	v_cndmask_b32_e32 v51, v51, v52, vcc
	v_cndmask_b32_e64 v51, v51, v60, s[20:21]
	v_lshlrev_b32_e32 v51, 2, v51
	ds_read_b32 v53, v51 offset:9728
	v_cmp_gt_i32_e64 s[20:21], 0, v29
	v_subrev_co_u32_e32 v51, vcc, 0x61a80, v29
	v_lshrrev_b32_e32 v51, 6, v51
	v_lshrrev_b32_e32 v52, 9, v29
	v_add_u32_e32 v51, 0x30e, v51
	v_cndmask_b32_e32 v51, v51, v52, vcc
	v_cndmask_b32_e64 v51, v51, v60, s[20:21]
	v_lshlrev_b32_e32 v51, 2, v51
	ds_read_b32 v54, v51 offset:9728
	v_cmp_gt_i32_e64 s[20:21], 0, v31
	v_subrev_co_u32_e32 v51, vcc, 0x61a80, v31
	v_lshrrev_b32_e32 v51, 6, v51
	v_lshrrev_b32_e32 v52, 9, v31
	v_add_u32_e32 v51, 0x30e, v51
	v_cndmask_b32_e32 v51, v51, v52, vcc
	v_cndmask_b32_e64 v51, v51, v60, s[20:21]
	v_lshlrev_b32_e32 v51, 2, v51
	ds_read_b32 v55, v51 offset:9728
	v_cmp_gt_i32_e64 s[20:21], 0, v33
	v_subrev_co_u32_e32 v51, vcc, 0x61a80, v33
	v_lshrrev_b32_e32 v51, 6, v51
	v_lshrrev_b32_e32 v52, 9, v33
	v_add_u32_e32 v51, 0x30e, v51
	v_cndmask_b32_e32 v51, v51, v52, vcc
	v_cndmask_b32_e64 v51, v51, v60, s[20:21]
	v_lshlrev_b32_e32 v51, 2, v51
	ds_read_b32 v56, v51 offset:9728
	s_waitcnt lgkmcnt(0)
	v_add_u32_e32 v46, v46, v53
	v_add_u32_e32 v47, v47, v54
	v_add_u32_e32 v48, v48, v55
	v_add_u32_e32 v49, v49, v56
	s_mov_b64 s[38:39], exec
	s_movk_i32 s14, 0x4000
	v_cmp_gt_u32_e32 vcc, s14, v34
	v_lshlrev_b32_e32 v52, 3, v34
	s_and_b64 exec, s[38:39], vcc
	ds_write_b64 v52, v[2:3] offset:14336
	s_mov_b64 exec, s[38:39]
	v_cmp_gt_u32_e32 vcc, s14, v35
	v_lshlrev_b32_e32 v52, 3, v35
	s_and_b64 exec, s[38:39], vcc
	ds_write_b64 v52, v[4:5] offset:14336
	s_mov_b64 exec, s[38:39]
	v_cmp_gt_u32_e32 vcc, s14, v36
	v_lshlrev_b32_e32 v52, 3, v36
	s_and_b64 exec, s[38:39], vcc
	ds_write_b64 v52, v[6:7] offset:14336
	s_mov_b64 exec, s[38:39]
	v_cmp_gt_u32_e32 vcc, s14, v37
	v_lshlrev_b32_e32 v52, 3, v37
	s_and_b64 exec, s[38:39], vcc
	ds_write_b64 v52, v[8:9] offset:14336
	s_mov_b64 exec, s[38:39]
	v_cmp_gt_u32_e32 vcc, s14, v38
	v_lshlrev_b32_e32 v52, 3, v38
	s_and_b64 exec, s[38:39], vcc
	ds_write_b64 v52, v[10:11] offset:14336
	s_mov_b64 exec, s[38:39]
	v_cmp_gt_u32_e32 vcc, s14, v39
	v_lshlrev_b32_e32 v52, 3, v39
	s_and_b64 exec, s[38:39], vcc
	ds_write_b64 v52, v[12:13] offset:14336
	s_mov_b64 exec, s[38:39]
	v_cmp_gt_u32_e32 vcc, s14, v40
	v_lshlrev_b32_e32 v52, 3, v40
	s_and_b64 exec, s[38:39], vcc
	ds_write_b64 v52, v[14:15] offset:14336
	s_mov_b64 exec, s[38:39]
	v_cmp_gt_u32_e32 vcc, s14, v41
	v_lshlrev_b32_e32 v52, 3, v41
	s_and_b64 exec, s[38:39], vcc
	ds_write_b64 v52, v[16:17] offset:14336
	s_mov_b64 exec, s[38:39]
	v_cmp_gt_u32_e32 vcc, s14, v42
	v_lshlrev_b32_e32 v52, 3, v42
	s_and_b64 exec, s[38:39], vcc
	ds_write_b64 v52, v[18:19] offset:14336
	s_mov_b64 exec, s[38:39]
	v_cmp_gt_u32_e32 vcc, s14, v43
	v_lshlrev_b32_e32 v52, 3, v43
	s_and_b64 exec, s[38:39], vcc
	ds_write_b64 v52, v[20:21] offset:14336
	s_mov_b64 exec, s[38:39]
	v_cmp_gt_u32_e32 vcc, s14, v44
	v_lshlrev_b32_e32 v52, 3, v44
	s_and_b64 exec, s[38:39], vcc
	ds_write_b64 v52, v[22:23] offset:14336
	s_mov_b64 exec, s[38:39]
	v_cmp_gt_u32_e32 vcc, s14, v45
	v_lshlrev_b32_e32 v52, 3, v45
	s_and_b64 exec, s[38:39], vcc
	ds_write_b64 v52, v[24:25] offset:14336
	s_mov_b64 exec, s[38:39]
	v_cmp_gt_u32_e32 vcc, s14, v46
	v_lshlrev_b32_e32 v52, 3, v46
	s_and_b64 exec, s[38:39], vcc
	ds_write_b64 v52, v[26:27] offset:14336
	s_mov_b64 exec, s[38:39]
	v_cmp_gt_u32_e32 vcc, s14, v47
	v_lshlrev_b32_e32 v52, 3, v47
	s_and_b64 exec, s[38:39], vcc
	ds_write_b64 v52, v[28:29] offset:14336
	s_mov_b64 exec, s[38:39]
	v_cmp_gt_u32_e32 vcc, s14, v48
	v_lshlrev_b32_e32 v52, 3, v48
	s_and_b64 exec, s[38:39], vcc
	ds_write_b64 v52, v[30:31] offset:14336
	s_mov_b64 exec, s[38:39]
	v_cmp_gt_u32_e32 vcc, s14, v49
	v_lshlrev_b32_e32 v52, 3, v49
	s_and_b64 exec, s[38:39], vcc
	ds_write_b64 v52, v[32:33] offset:14336
	s_mov_b64 exec, s[38:39]
	s_waitcnt lgkmcnt(0)
	s_barrier
	v_lshlrev_b32_e32 v62, 3, v0
	ds_read_b64 v[2:3], v62 offset:14336
	v_add_u32_e32 v63, 0x2000, v62
	ds_read_b64 v[4:5], v63 offset:14336
	v_add_u32_e32 v63, 0x4000, v62
	ds_read_b64 v[6:7], v63 offset:14336
	v_add_u32_e32 v63, 0x6000, v62
	ds_read_b64 v[8:9], v63 offset:14336
	v_add_u32_e32 v63, 0x8000, v62
	ds_read_b64 v[10:11], v63 offset:14336
	v_add_u32_e32 v63, 0xa000, v62
	ds_read_b64 v[12:13], v63 offset:14336
	v_add_u32_e32 v63, 0xc000, v62
	ds_read_b64 v[14:15], v63 offset:14336
	v_add_u32_e32 v63, 0xe000, v62
	ds_read_b64 v[16:17], v63 offset:14336
	v_add_u32_e32 v63, 0x10000, v62
	ds_read_b64 v[18:19], v63 offset:14336
	v_add_u32_e32 v63, 0x12000, v62
	ds_read_b64 v[20:21], v63 offset:14336
	v_add_u32_e32 v63, 0x14000, v62
	ds_read_b64 v[22:23], v63 offset:14336
	v_add_u32_e32 v63, 0x16000, v62
	ds_read_b64 v[24:25], v63 offset:14336
	v_add_u32_e32 v63, 0x18000, v62
	ds_read_b64 v[26:27], v63 offset:14336
	v_add_u32_e32 v63, 0x1a000, v62
	ds_read_b64 v[28:29], v63 offset:14336
	v_add_u32_e32 v63, 0x1c000, v62
	ds_read_b64 v[30:31], v63 offset:14336
	v_add_u32_e32 v63, 0x1e000, v62
	ds_read_b64 v[32:33], v63 offset:14336
	s_waitcnt lgkmcnt(0)
	v_subrev_co_u32_e32 v34, vcc, 0x61a80, v3
	v_lshrrev_b32_e32 v34, 6, v34
	v_lshrrev_b32_e32 v50, 9, v3
	v_add_u32_e32 v34, 0x30e, v34
	v_cndmask_b32_e32 v34, v34, v50, vcc
	v_min_u32_e32 v34, 0x447, v34
	v_lshlrev_b32_e32 v34, 2, v34
	ds_read_b32 v34, v34
	v_subrev_co_u32_e32 v35, vcc, 0x61a80, v5
	v_lshrrev_b32_e32 v35, 6, v35
	v_lshrrev_b32_e32 v50, 9, v5
	v_add_u32_e32 v35, 0x30e, v35
	v_cndmask_b32_e32 v35, v35, v50, vcc
	v_min_u32_e32 v35, 0x447, v35
	v_lshlrev_b32_e32 v35, 2, v35
	ds_read_b32 v35, v35
	v_subrev_co_u32_e32 v36, vcc, 0x61a80, v7
	v_lshrrev_b32_e32 v36, 6, v36
	v_lshrrev_b32_e32 v50, 9, v7
	v_add_u32_e32 v36, 0x30e, v36
	v_cndmask_b32_e32 v36, v36, v50, vcc
	v_min_u32_e32 v36, 0x447, v36
	v_lshlrev_b32_e32 v36, 2, v36
	ds_read_b32 v36, v36
	v_subrev_co_u32_e32 v37, vcc, 0x61a80, v9
	v_lshrrev_b32_e32 v37, 6, v37
	v_lshrrev_b32_e32 v50, 9, v9
	v_add_u32_e32 v37, 0x30e, v37
	v_cndmask_b32_e32 v37, v37, v50, vcc
	v_min_u32_e32 v37, 0x447, v37
	v_lshlrev_b32_e32 v37, 2, v37
	ds_read_b32 v37, v37
	v_subrev_co_u32_e32 v38, vcc, 0x61a80, v11
	v_lshrrev_b32_e32 v38, 6, v38
	v_lshrrev_b32_e32 v50, 9, v11
	v_add_u32_e32 v38, 0x30e, v38
	v_cndmask_b32_e32 v38, v38, v50, vcc
	v_min_u32_e32 v38, 0x447, v38
	v_lshlrev_b32_e32 v38, 2, v38
	ds_read_b32 v38, v38
	v_subrev_co_u32_e32 v39, vcc, 0x61a80, v13
	v_lshrrev_b32_e32 v39, 6, v39
	v_lshrrev_b32_e32 v50, 9, v13
	v_add_u32_e32 v39, 0x30e, v39
	v_cndmask_b32_e32 v39, v39, v50, vcc
	v_min_u32_e32 v39, 0x447, v39
	v_lshlrev_b32_e32 v39, 2, v39
	ds_read_b32 v39, v39
	v_subrev_co_u32_e32 v40, vcc, 0x61a80, v15
	v_lshrrev_b32_e32 v40, 6, v40
	v_lshrrev_b32_e32 v50, 9, v15
	v_add_u32_e32 v40, 0x30e, v40
	v_cndmask_b32_e32 v40, v40, v50, vcc
	v_min_u32_e32 v40, 0x447, v40
	v_lshlrev_b32_e32 v40, 2, v40
	ds_read_b32 v40, v40
	v_subrev_co_u32_e32 v41, vcc, 0x61a80, v17
	v_lshrrev_b32_e32 v41, 6, v41
	v_lshrrev_b32_e32 v50, 9, v17
	v_add_u32_e32 v41, 0x30e, v41
	v_cndmask_b32_e32 v41, v41, v50, vcc
	v_min_u32_e32 v41, 0x447, v41
	v_lshlrev_b32_e32 v41, 2, v41
	ds_read_b32 v41, v41
	v_subrev_co_u32_e32 v42, vcc, 0x61a80, v19
	v_lshrrev_b32_e32 v42, 6, v42
	v_lshrrev_b32_e32 v50, 9, v19
	v_add_u32_e32 v42, 0x30e, v42
	v_cndmask_b32_e32 v42, v42, v50, vcc
	v_min_u32_e32 v42, 0x447, v42
	v_lshlrev_b32_e32 v42, 2, v42
	ds_read_b32 v42, v42
	v_subrev_co_u32_e32 v43, vcc, 0x61a80, v21
	v_lshrrev_b32_e32 v43, 6, v43
	v_lshrrev_b32_e32 v50, 9, v21
	v_add_u32_e32 v43, 0x30e, v43
	v_cndmask_b32_e32 v43, v43, v50, vcc
	v_min_u32_e32 v43, 0x447, v43
	v_lshlrev_b32_e32 v43, 2, v43
	ds_read_b32 v43, v43
	v_subrev_co_u32_e32 v44, vcc, 0x61a80, v23
	v_lshrrev_b32_e32 v44, 6, v44
	v_lshrrev_b32_e32 v50, 9, v23
	v_add_u32_e32 v44, 0x30e, v44
	v_cndmask_b32_e32 v44, v44, v50, vcc
	v_min_u32_e32 v44, 0x447, v44
	v_lshlrev_b32_e32 v44, 2, v44
	ds_read_b32 v44, v44
	v_subrev_co_u32_e32 v45, vcc, 0x61a80, v25
	v_lshrrev_b32_e32 v45, 6, v45
	v_lshrrev_b32_e32 v50, 9, v25
	v_add_u32_e32 v45, 0x30e, v45
	v_cndmask_b32_e32 v45, v45, v50, vcc
	v_min_u32_e32 v45, 0x447, v45
	v_lshlrev_b32_e32 v45, 2, v45
	ds_read_b32 v45, v45
	v_subrev_co_u32_e32 v46, vcc, 0x61a80, v27
	v_lshrrev_b32_e32 v46, 6, v46
	v_lshrrev_b32_e32 v50, 9, v27
	v_add_u32_e32 v46, 0x30e, v46
	v_cndmask_b32_e32 v46, v46, v50, vcc
	v_min_u32_e32 v46, 0x447, v46
	v_lshlrev_b32_e32 v46, 2, v46
	ds_read_b32 v46, v46
	v_subrev_co_u32_e32 v47, vcc, 0x61a80, v29
	v_lshrrev_b32_e32 v47, 6, v47
	v_lshrrev_b32_e32 v50, 9, v29
	v_add_u32_e32 v47, 0x30e, v47
	v_cndmask_b32_e32 v47, v47, v50, vcc
	v_min_u32_e32 v47, 0x447, v47
	v_lshlrev_b32_e32 v47, 2, v47
	ds_read_b32 v47, v47
	v_subrev_co_u32_e32 v48, vcc, 0x61a80, v31
	v_lshrrev_b32_e32 v48, 6, v48
	v_lshrrev_b32_e32 v50, 9, v31
	v_add_u32_e32 v48, 0x30e, v48
	v_cndmask_b32_e32 v48, v48, v50, vcc
	v_min_u32_e32 v48, 0x447, v48
	v_lshlrev_b32_e32 v48, 2, v48
	ds_read_b32 v48, v48
	v_subrev_co_u32_e32 v49, vcc, 0x61a80, v33
	v_lshrrev_b32_e32 v49, 6, v49
	v_lshrrev_b32_e32 v50, 9, v33
	v_add_u32_e32 v49, 0x30e, v49
	v_cndmask_b32_e32 v49, v49, v50, vcc
	v_min_u32_e32 v49, 0x447, v49
	v_lshlrev_b32_e32 v49, 2, v49
	ds_read_b32 v49, v49
	s_waitcnt lgkmcnt(0)
	v_mov_b32_e32 v51, v0
	v_cmp_le_i32_e32 vcc, 0, v3
	v_add_u32_e32 v34, v34, v51
	v_lshlrev_b32_e32 v34, 3, v34
	s_and_b64 exec, s[38:39], vcc
	global_store_dwordx2 v34, v[2:3], s[34:35]
	s_mov_b64 exec, s[38:39]
	v_add_u32_e32 v51, 0x400, v0
	v_cmp_le_i32_e32 vcc, 0, v5
	v_add_u32_e32 v35, v35, v51
	v_lshlrev_b32_e32 v35, 3, v35
	s_and_b64 exec, s[38:39], vcc
	global_store_dwordx2 v35, v[4:5], s[34:35]
	s_mov_b64 exec, s[38:39]
	v_add_u32_e32 v51, 0x800, v0
	v_cmp_le_i32_e32 vcc, 0, v7
	v_add_u32_e32 v36, v36, v51
	v_lshlrev_b32_e32 v36, 3, v36
	s_and_b64 exec, s[38:39], vcc
	global_store_dwordx2 v36, v[6:7], s[34:35]
	s_mov_b64 exec, s[38:39]
	v_add_u32_e32 v51, 0xc00, v0
	v_cmp_le_i32_e32 vcc, 0, v9
	v_add_u32_e32 v37, v37, v51
	v_lshlrev_b32_e32 v37, 3, v37
	s_and_b64 exec, s[38:39], vcc
	global_store_dwordx2 v37, v[8:9], s[34:35]
	s_mov_b64 exec, s[38:39]
	v_add_u32_e32 v51, 0x1000, v0
	v_cmp_le_i32_e32 vcc, 0, v11
	v_add_u32_e32 v38, v38, v51
	v_lshlrev_b32_e32 v38, 3, v38
	s_and_b64 exec, s[38:39], vcc
	global_store_dwordx2 v38, v[10:11], s[34:35]
	s_mov_b64 exec, s[38:39]
	v_add_u32_e32 v51, 0x1400, v0
	v_cmp_le_i32_e32 vcc, 0, v13
	v_add_u32_e32 v39, v39, v51
	v_lshlrev_b32_e32 v39, 3, v39
	s_and_b64 exec, s[38:39], vcc
	global_store_dwordx2 v39, v[12:13], s[34:35]
	s_mov_b64 exec, s[38:39]
	v_add_u32_e32 v51, 0x1800, v0
	v_cmp_le_i32_e32 vcc, 0, v15
	v_add_u32_e32 v40, v40, v51
	v_lshlrev_b32_e32 v40, 3, v40
	s_and_b64 exec, s[38:39], vcc
	global_store_dwordx2 v40, v[14:15], s[34:35]
	s_mov_b64 exec, s[38:39]
	v_add_u32_e32 v51, 0x1c00, v0
	v_cmp_le_i32_e32 vcc, 0, v17
	v_add_u32_e32 v41, v41, v51
	v_lshlrev_b32_e32 v41, 3, v41
	s_and_b64 exec, s[38:39], vcc
	global_store_dwordx2 v41, v[16:17], s[34:35]
	s_mov_b64 exec, s[38:39]
	v_add_u32_e32 v51, 0x2000, v0
	v_cmp_le_i32_e32 vcc, 0, v19
	v_add_u32_e32 v42, v42, v51
	v_lshlrev_b32_e32 v42, 3, v42
	s_and_b64 exec, s[38:39], vcc
	global_store_dwordx2 v42, v[18:19], s[34:35]
	s_mov_b64 exec, s[38:39]
	v_add_u32_e32 v51, 0x2400, v0
	v_cmp_le_i32_e32 vcc, 0, v21
	v_add_u32_e32 v43, v43, v51
	v_lshlrev_b32_e32 v43, 3, v43
	s_and_b64 exec, s[38:39], vcc
	global_store_dwordx2 v43, v[20:21], s[34:35]
	s_mov_b64 exec, s[38:39]
	v_add_u32_e32 v51, 0x2800, v0
	v_cmp_le_i32_e32 vcc, 0, v23
	v_add_u32_e32 v44, v44, v51
	v_lshlrev_b32_e32 v44, 3, v44
	s_and_b64 exec, s[38:39], vcc
	global_store_dwordx2 v44, v[22:23], s[34:35]
	s_mov_b64 exec, s[38:39]
	v_add_u32_e32 v51, 0x2c00, v0
	v_cmp_le_i32_e32 vcc, 0, v25
	v_add_u32_e32 v45, v45, v51
	v_lshlrev_b32_e32 v45, 3, v45
	s_and_b64 exec, s[38:39], vcc
	global_store_dwordx2 v45, v[24:25], s[34:35]
	s_mov_b64 exec, s[38:39]
	v_add_u32_e32 v51, 0x3000, v0
	v_cmp_le_i32_e32 vcc, 0, v27
	v_add_u32_e32 v46, v46, v51
	v_lshlrev_b32_e32 v46, 3, v46
	s_and_b64 exec, s[38:39], vcc
	global_store_dwordx2 v46, v[26:27], s[34:35]
	s_mov_b64 exec, s[38:39]
	v_add_u32_e32 v51, 0x3400, v0
	v_cmp_le_i32_e32 vcc, 0, v29
	v_add_u32_e32 v47, v47, v51
	v_lshlrev_b32_e32 v47, 3, v47
	s_and_b64 exec, s[38:39], vcc
	global_store_dwordx2 v47, v[28:29], s[34:35]
	s_mov_b64 exec, s[38:39]
	v_add_u32_e32 v51, 0x3800, v0
	v_cmp_le_i32_e32 vcc, 0, v31
	v_add_u32_e32 v48, v48, v51
	v_lshlrev_b32_e32 v48, 3, v48
	s_and_b64 exec, s[38:39], vcc
	global_store_dwordx2 v48, v[30:31], s[34:35]
	s_mov_b64 exec, s[38:39]
	v_add_u32_e32 v51, 0x3c00, v0
	v_cmp_le_i32_e32 vcc, 0, v33
	v_add_u32_e32 v49, v49, v51
	v_lshlrev_b32_e32 v49, 3, v49
	s_and_b64 exec, s[38:39], vcc
	global_store_dwordx2 v49, v[32:33], s[34:35]
	s_mov_b64 exec, s[38:39]
	s_endpgm
